# mixer work queue: only Q-blocks below 12 split into half items (was 16), whole items 63..12; on top of v26
# baseline (speedup 1.0000x reference)
.LBB0_455:
	v_readlane_b32 s12, v251, 0
	v_readlane_b32 s14, v251, 2
	v_readlane_b32 s15, v251, 3
	s_add_u32 s60, s14, s62
	s_addc_u32 s61, s15, s63
	s_lshl_b32 s4, s0, 9
	s_ashr_i32 s5, s4, 31
	s_lshl_b64 s[4:5], s[4:5], 2
	v_readlane_b32 s1, v252, 14
	s_add_u32 s34, s1, s4
	v_readlane_b32 s1, v252, 15
	s_addc_u32 s35, s1, s5
	s_cmp_lt_i32 s0, 3
	s_movk_i32 s1, 0x73
	s_cselect_b32 s15, s1, 0x54
	v_readlane_b32 s1, v252, 16
	s_add_u32 s4, s1, s62
	v_readlane_b32 s1, v252, 17
	s_addc_u32 s5, s1, s63
	s_add_u32 s1, s60, 0x1ec00000
	v_writelane_b32 v254, s1, 34
	s_addc_u32 s1, s61, 0
	s_add_u32 s74, s60, 0xac00000
	s_addc_u32 s75, s61, 0
	v_readlane_b32 s13, v251, 1
	s_add_u32 s12, s60, 0x5f00000
	v_writelane_b32 v254, s1, 35
	s_addc_u32 s13, s61, 0
	v_writelane_b32 v254, s12, 36
	v_readlane_b32 s16, v251, 11
	v_readlane_b32 s30, v251, 25
	v_writelane_b32 v254, s13, 37
	v_readlane_b32 s12, v253, 46
	v_readlane_b32 s13, v253, 47
	s_add_u32 s12, s4, s12
	s_addc_u32 s13, s5, s13
	v_writelane_b32 v254, s12, 38
	s_add_u32 s1, s60, 0x1a800000
	v_readlane_b32 s24, v251, 19
	v_writelane_b32 v254, s13, 39
	v_writelane_b32 v254, s1, 40
	s_addc_u32 s1, s61, 0
	v_writelane_b32 v254, s1, 41
	s_add_u32 s1, s60, 0x1a000000
	v_writelane_b32 v254, s1, 42
	s_addc_u32 s1, s61, 0
	v_writelane_b32 v254, s1, 43
	v_readlane_b32 s25, v251, 20
	v_readlane_b32 s12, v254, 16
	v_readlane_b32 s13, v254, 17
	s_add_u32 s1, s60, s12
	s_addc_u32 s12, s61, s13
	s_add_u32 s1, s1, 0x1ba00000
	v_writelane_b32 v254, s1, 44
	s_addc_u32 s1, s12, 0
	v_writelane_b32 v254, s1, 45
	s_lshl_b32 s1, s0, 10
	s_add_u32 s12, s60, 0x6100200
	v_writelane_b32 v254, s1, 46
	s_addc_u32 s13, s61, 0
	v_writelane_b32 v254, s12, 47
	s_add_u32 s1, s60, 0x17d00000
	v_readlane_b32 s31, v251, 26
	v_writelane_b32 v254, s13, 48
	v_writelane_b32 v254, s1, 49
	s_addc_u32 s1, s61, 0
	v_writelane_b32 v254, s1, 50
	s_add_u32 s1, s60, 0x17c00000
	v_writelane_b32 v254, s1, 51
	s_addc_u32 s1, s61, 0
	s_add_u32 s58, s60, 0x1da00000
	s_addc_u32 s59, s61, 0
	s_add_u32 s40, s60, 0x5e00000
	v_writelane_b32 v254, s1, 52
	s_addc_u32 s41, s61, 0
	s_ashr_i32 s1, s0, 31
	s_lshl_b64 s[12:13], s[0:1], 10
	s_add_u32 s1, s30, s12
	s_mov_b64 s[24:25], s[40:41]
	v_writelane_b32 v254, s1, 53
	s_addc_u32 s1, s31, s13
	s_add_i32 s12, s0, 1
	v_readlane_b32 s40, v251, 30
	v_writelane_b32 v254, s1, 54
	s_mul_i32 s1, s12, 0x1600000
	v_readlane_b32 s42, v251, 32
	v_readlane_b32 s17, v251, 12
	s_mul_hi_i32 s0, s12, 0x1600000
	v_readlane_b32 s43, v251, 33
	s_add_u32 s16, s42, s1
	s_addc_u32 s17, s43, s0
	s_lshl_b32 s0, s12, 10
	s_ashr_i32 s1, s0, 31
	v_readlane_b32 s22, v251, 17
	s_lshl_b64 s[0:1], s[0:1], 2
	v_readlane_b32 s23, v251, 18
	v_readlane_b32 s41, v251, 31
	s_add_u32 s22, s40, s0
	s_addc_u32 s23, s41, s1
	s_mul_i32 s13, s12, 0x580000
	s_add_u32 s13, s60, s13
	s_mul_hi_i32 s14, s12, 0x580000
	v_writelane_b32 v254, s16, 55
	s_addc_u32 s14, s61, s14
	v_readlane_b32 s44, v251, 34
	v_writelane_b32 v254, s17, 56
	s_add_u32 s16, s13, 0x18200000
	s_addc_u32 s17, s14, 0
	s_mul_i32 s13, s12, 0x5800
	s_add_u32 s13, s60, s13
	s_mul_hi_i32 s14, s12, 0x5800
	v_readlane_b32 s45, v251, 35
	v_readlane_b32 s46, v251, 36
	v_readlane_b32 s47, v251, 37
	v_writelane_b32 v254, s16, 57
	s_addc_u32 s14, s61, s14
	s_add_u32 s13, s13, 0x5300000
	v_writelane_b32 v254, s17, 58
	v_readlane_b32 s40, v251, 53
	v_writelane_b32 v254, s13, 59
	s_addc_u32 s13, s14, 0
	s_mul_i32 s14, s12, 0x8c4000
	v_readlane_b32 s42, v251, 55
	v_writelane_b32 v254, s13, 60
	s_mul_hi_i32 s13, s12, 0x8c4000
	v_readlane_b32 s43, v251, 56
	v_readlane_b32 s54, v252, 3
	s_add_u32 s14, s42, s14
	s_mov_b32 s54, s15
	s_addc_u32 s15, s43, s13
	v_readlane_b32 s46, v251, 59
	v_writelane_b32 v254, s14, 61
	v_readlane_b32 s47, v251, 60
	v_readlane_b32 s52, v252, 1
	v_writelane_b32 v254, s15, 62
	s_add_u32 s14, s46, s0
	s_addc_u32 s15, s47, s1
	s_mul_i32 s0, s12, 0x240000
	s_add_u32 s0, s60, s0
	s_mul_hi_i32 s1, s12, 0x240000
	s_addc_u32 s1, s61, s1
	s_add_u32 s0, s0, 0x5500000
	s_addc_u32 s1, s1, 0
	v_writelane_b32 v254, s0, 63
	v_readlane_b32 s53, v252, 2
	s_mov_b64 s[52:53], s[34:35]
	v_writelane_b32 v255, s1, 0
	s_mul_hi_i32 s0, s12, 0x2400
	s_mulk_i32 s12, 0x2400
	s_add_u32 s1, s60, s12
	s_addc_u32 s0, s61, s0
	s_add_u32 s1, s1, 0x5320000
	v_writelane_b32 v255, s1, 1
	s_addc_u32 s0, s0, 0
	v_writelane_b32 v255, s0, 2
	v_readlane_b32 s0, v253, 39
	s_add_u32 s12, s0, s62
	v_readlane_b32 s0, v253, 40
	s_addc_u32 s13, s0, s63
	v_writelane_b32 v255, s12, 3
	v_readlane_b32 s0, v254, 6
	v_readlane_b32 s18, v251, 13
	v_writelane_b32 v255, s13, 4
	s_add_u32 s12, s0, s62
	v_readlane_b32 s0, v254, 7
	s_addc_u32 s13, s0, s63
	v_writelane_b32 v255, s12, 5
	v_readlane_b32 s0, v254, 12
	s_add_u32 s0, s0, s62
	v_writelane_b32 v255, s13, 6
	v_writelane_b32 v255, s0, 7
	v_readlane_b32 s0, v254, 13
	s_addc_u32 s0, s0, s63
	v_readlane_b32 s19, v251, 14
	v_writelane_b32 v255, s0, 8
	v_readlane_b32 s0, v254, 14
	s_add_u32 s0, s0, s62
	v_readlane_b32 s20, v251, 15
	v_writelane_b32 v255, s0, 9
	v_readlane_b32 s0, v254, 15
	s_addc_u32 s0, s0, s63
	v_readlane_b32 s21, v251, 16
	v_writelane_b32 v255, s0, 10
	v_writelane_b32 v255, s24, 11
	v_readlane_b32 s26, v251, 21
	v_readlane_b32 s27, v251, 22
	v_writelane_b32 v255, s25, 12
	v_readlane_b32 s28, v251, 23
	v_readlane_b32 s29, v251, 24
	v_readlane_b32 s41, v251, 54
	v_readlane_b32 s44, v251, 57
	v_readlane_b32 s45, v251, 58
	v_readlane_b32 s48, v251, 61
	v_readlane_b32 s49, v251, 62
	v_readlane_b32 s50, v251, 63
	v_readlane_b32 s51, v252, 0
	v_readlane_b32 s55, v252, 4
	s_branch .LBB0_459

.LBB0_476:
	v_readlane_b32 s0, v254, 24
	s_waitcnt lgkmcnt(0)
	s_barrier
	v_mov_b32_e32 v0, s0
	ds_read_b32 v0, v0
	s_waitcnt lgkmcnt(0)
	v_readfirstlane_b32 s48, v0
	s_cmp_eq_u32 s48, -1
	s_cbranch_scc1 .LBB0_509
	s_lshr_b32 s19, s48, 8
	s_and_b32 s57, s48, 0xff
	s_cmpk_lt_u32 s57, 0x54
	s_mov_b64 s[0:1], -1
	s_cbranch_scc0 .LBB0_846
	s_and_b32 s0, s48, 0xfc
	s_cmp_lg_u32 s0, 4
	s_mov_b64 s[0:1], -1
	s_cbranch_scc0 .LBB0_830
	s_cmp_gt_u32 s57, 3
	s_cbranch_scc0 .LBB0_797
	s_cmp_gt_u32 s57, 59
	s_cbranch_scc0 .LBB0_767
	s_sub_i32 s0, s57, 60
	s_lshr_b32 s0, s0, 1
	s_sub_i32 s30, 11, s0
	s_and_b32 s18, s48, 1
	s_mov_b32 s44, s19
	v_mov_b32_e32 v0, v1
	s_ashr_i32 s45, s44, 31
	v_mbcnt_lo_u32_b32 v0, -1, v0
	v_mbcnt_hi_u32_b32 v42, -1, v0
	v_add_u32_e32 v2, s94, v42
	s_lshl_b64 s[0:1], s[44:45], 21
	v_readlane_b32 s12, v254, 34
	v_ashrrev_i32_e32 v4, 2, v2
	s_add_u32 s42, s12, s0
	v_readlane_b32 s0, v254, 35
	v_ashrrev_i32_e32 v5, 31, v4
	s_addc_u32 s43, s0, s1
	v_lshlrev_b64 v[4:5], 9, v[4:5]
	v_lshlrev_b32_e32 v0, 5, v42
	v_lshl_add_u64 v[4:5], s[42:43], 0, v[4:5]
	v_and_b32_e32 v0, 0x60, v0
	v_lshl_add_u64 v[8:9], v[4:5], 0, v[0:1]
	global_load_dwordx4 v[4:7], v[8:9], off offset:272
	s_nop 0
	global_load_dwordx4 v[8:11], v[8:9], off offset:256
	v_cmp_eq_u32_e64 s[26:27], 0, v42
	s_waitcnt vmcnt(0)
	v_and_b32_e32 v3, 0xffff0000, v8
	v_lshlrev_b32_e32 v0, 16, v8
	v_mul_f32_e32 v3, v3, v3
	v_and_b32_e32 v8, 0xffff0000, v9
	v_fmac_f32_e32 v3, v0, v0
	v_lshlrev_b32_e32 v0, 16, v9
	v_mul_f32_e32 v8, v8, v8
	v_fmac_f32_e32 v8, v0, v0
	v_add_f32_e32 v0, v3, v8
	v_and_b32_e32 v8, 0xffff0000, v10
	v_lshlrev_b32_e32 v3, 16, v10
	v_mul_f32_e32 v8, v8, v8
	v_fmac_f32_e32 v8, v3, v3
	v_add_f32_e32 v0, v8, v0
	v_and_b32_e32 v8, 0xffff0000, v11
	v_lshlrev_b32_e32 v3, 16, v11
	v_mul_f32_e32 v8, v8, v8
	v_fmac_f32_e32 v8, v3, v3
	v_lshlrev_b32_e32 v3, 16, v4
	v_and_b32_e32 v4, 0xffff0000, v4
	v_mul_f32_e32 v4, v4, v4
	v_add_f32_e32 v0, v8, v0
	v_fmac_f32_e32 v4, v3, v3
	v_add_f32_e32 v0, v4, v0
	v_and_b32_e32 v4, 0xffff0000, v5
	v_lshlrev_b32_e32 v3, 16, v5
	v_mul_f32_e32 v4, v4, v4
	v_fmac_f32_e32 v4, v3, v3
	v_add_f32_e32 v0, v4, v0
	v_and_b32_e32 v4, 0xffff0000, v6
	v_lshlrev_b32_e32 v3, 16, v6
	v_mul_f32_e32 v4, v4, v4
	v_fmac_f32_e32 v4, v3, v3
	v_add_f32_e32 v0, v4, v0
	v_and_b32_e32 v4, 0xffff0000, v7
	v_lshlrev_b32_e32 v3, 16, v7
	v_mul_f32_e32 v4, v4, v4
	v_fmac_f32_e32 v4, v3, v3
	v_add_f32_e32 v0, v4, v0
	s_nop 1
	v_add_f32_dpp v0, v0, v0 quad_perm:[1,0,3,2] row_mask:0xf bank_mask:0xf bound_ctrl:1
	s_nop 1
	v_add_f32_dpp v0, v0, v0 quad_perm:[2,3,0,1] row_mask:0xf bank_mask:0xf bound_ctrl:1
	s_nop 1
	v_add_f32_dpp v0, v0, v0 row_half_mirror row_mask:0xf bank_mask:0xf bound_ctrl:1
	s_nop 1
	v_add_f32_dpp v0, v0, v0 row_mirror row_mask:0xf bank_mask:0xf bound_ctrl:1
	v_mov_b32_e32 v3, v0
	s_nop 1
	v_permlane16_swap_b32_e32 v0, v3
	v_add_f32_e32 v0, v0, v3
	v_mov_b32_e32 v3, v0
	s_nop 1
	v_permlane32_swap_b32_e32 v0, v3
	s_and_saveexec_b64 s[0:1], s[26:27]
	s_cbranch_execz .LBB0_483
	v_readlane_b32 s12, v252, 18
	v_add_f32_e32 v0, v0, v3
	s_nop 0
	v_mov_b32_e32 v3, s12
	ds_write_b32 v3, v0

.LBB0_846:
	s_andn2_b64 vcc, exec, s[0:1]
	s_cbranch_vccnz .LBB0_458
	s_mul_i32 s0, s19, 31
	s_add_i32 s12, s57, s0
	s_addk_i32 s12, 0xffac
	s_lshl_b32 s18, s12, 5
	s_cmpk_gt_u32 s12, 0x47
	s_mov_b64 s[0:1], -1
	s_cbranch_scc0 .LBB0_861
	v_mov_b32_e32 v0, v1
	v_readlane_b32 s0, v251, 4
	v_mbcnt_lo_u32_b32 v0, -1, v0
	v_mbcnt_hi_u32_b32 v4, -1, v0
	v_cmp_gt_i32_e32 vcc, 32, v4
	v_readlane_b32 s1, v251, 5
	s_and_b64 s[26:27], s[0:1], vcc
	s_waitcnt vmcnt(0)
	s_barrier
	s_and_saveexec_b64 s[0:1], s[26:27]
	v_lshl_add_u32 v0, v4, 2, 0
	v_add_u32_e32 v0, 0x20200, v0
	ds_write_b32 v0, v1
	s_or_b64 exec, exec, s[0:1]
	s_add_i32 s13, s18, 0xfffff700
	s_and_b32 s0, s18, 0xe0
	v_and_b32_e32 v5, 31, v4
	s_cmpk_lt_u32 s0, 0x80
	v_or_b32_e32 v0, s0, v5
	s_cselect_b64 vcc, -1, 0
	s_lshr_b32 s0, s13, 1
	s_and_b32 s0, s0, 0x3fffff80
	v_or_b32_e32 v2, s0, v0
	s_addk_i32 s0, 0xa80
	v_add_u32_e32 v0, s0, v0
	v_readlane_b32 s0, v254, 55
	v_cndmask_b32_e32 v0, v0, v2, vcc
	v_readlane_b32 s1, v254, 56
	v_ashrrev_i32_e32 v7, 5, v4
	v_bfe_u32 v6, v4, 3, 2
	v_lshl_add_u64 v[2:3], v[0:1], 2, s[0:1]
	s_movk_i32 s0, 0x1010
	v_mad_u32_u24 v0, v5, s0, 0
	v_readlane_b32 s0, v252, 6
	v_mov_b32_e32 v8, 0
	s_waitcnt lgkmcnt(0)
	v_add_u32_e32 v7, s0, v7
	s_mov_b32 s0, 0
	s_barrier
